# two-block item: C-operand fills, exponentials and bf16 packs placed in the shadows of the MFMAs (keys 0..31 of a block go to the row-sum / PV MFMAs while the other half of its softmax runs)
# speedup vs baseline: 1.0035x; 1.0035x over previous
; __device__ __forceinline__ float ex2(float x) { return __builtin_amdgcn_exp2f(x); }
; template <bool SELMASK>
; __device__ __forceinline__ void attn_far_fast(const LAS unsigned char* kb, const LAS unsigned char* vb, const bf16x8 (&qf)[2][2], int col, int q, float bias_far, bool sel0, bool sel1, Softmax (&st)[2], f32x4 (&O)[2][4]) {
;     ...
; #pragma unroll
;     for (int kt = 0; kt < 4; ++kt) { const bf16x8 k0 = lds_frag(kb, 16 * kt + col, q), k1 = lds_frag(kb, 16 * kt + col, 4 + q);
; #pragma unroll
;         for (int c = 0; c < 2; ++c) { S[c][kt] = __builtin_amdgcn_mfma_f32_16x16x32_bf16(k0, qf[c][0], z4, 0, 0, 0); S[c][kt] = __builtin_amdgcn_mfma_f32_16x16x32_bf16(k1, qf[c][1], S[c][kt], 0, 0, 0); } }
;     bf16x8 pf[2][2];
; #pragma unroll
;     for (int c = 0; c < 2; ++c) {
;         const bool sel = c == 0 ? sel0 : sel1;
;         const float off = ((SELMASK && !sel) ? NEG : bias_far) - st[c].m;
; #pragma unroll
;         for (int kt = 0; kt < 4; ++kt) { f32x4 p = S[c][kt] + off;
; #pragma unroll
;             for (int e = 0; e < 4; ++e) p[e] = ex2(p[e]);
;             S[c][kt] = p; }
;         pf[c][0] = pack8(S[c][0], S[c][1]); pf[c][1] = pack8(S[c][2], S[c][3]);
;         st[c].l = __builtin_amdgcn_mfma_f32_16x16x32_bf16(ONES8, pf[c][0], st[c].l, 0, 0, 0); st[c].l = __builtin_amdgcn_mfma_f32_16x16x32_bf16(ONES8, pf[c][1], st[c].l, 0, 0, 0);
;     }
.Lbm_full_f:
	v_add_u32_e32 v148, s83, v192
	v_add_u32_e32 v149, v148, v195
	v_add_u32_e32 v148, v148, v193
	ds_read_b128 v[116:119], v148
	ds_read_b128 v[120:123], v149
	ds_read_b128 v[124:127], v148 offset:2048
	ds_read_b128 v[128:131], v149 offset:2048
	ds_read_b128 v[132:135], v148 offset:4096
	ds_read_b128 v[136:139], v149 offset:4096
	ds_read_b128 v[140:143], v148 offset:6144
	ds_read_b128 v[144:147], v149 offset:6144
	s_add_i32 s32, s1, 0x2000
	s_and_b32 s32, s32, 0x6000
	v_add_u32_e32 v208, s32, v192
	v_add_u32_e32 v209, v208, v195
	v_add_u32_e32 v208, v208, v193
	ds_read_b128 v[38:41], v208
	ds_read_b128 v[42:45], v209
	ds_read_b128 v[46:49], v208 offset:2048
	ds_read_b128 v[50:53], v209 offset:2048
	s_waitcnt lgkmcnt(12)
	v_sub_f32_e32 v81, v81, v199
	v_sub_f32_e32 v82, v82, v199
	v_mov_b32_e32 v70, v81
	v_mov_b32_e32 v71, v81
	v_mov_b32_e32 v72, v81
	v_mov_b32_e32 v73, v81
	v_mov_b32_e32 v74, v81
	v_mov_b32_e32 v75, v81
	v_mov_b32_e32 v76, v81
	v_mov_b32_e32 v77, v81
	v_mov_b32_e32 v200, v81
	v_mov_b32_e32 v201, v81
	v_mov_b32_e32 v202, v81
	v_mov_b32_e32 v203, v81
	v_mov_b32_e32 v204, v81
	v_mov_b32_e32 v205, v81
	v_mov_b32_e32 v206, v81
	v_mov_b32_e32 v207, v81
	s_mov_b32 s83, -1
	s_add_i32 s77, s75, 2
	s_cmp_gt_i32 s77, s26
	s_cbranch_scc1 .Lbm_g1_end_af
	s_lshr_b32 s21, s77, 5
	v_mov_b32_e32 v255, v242
	s_cmp_eq_u32 s21, 1
	s_cselect_b64 vcc, -1, 0
	v_cndmask_b32_e32 v255, v255, v243, vcc
	s_cmp_eq_u32 s21, 2
	s_cselect_b64 vcc, -1, 0
	v_cndmask_b32_e32 v255, v255, v244, vcc
	s_cmp_eq_u32 s21, 3
	s_cselect_b64 vcc, -1, 0
	v_cndmask_b32_e32 v255, v255, v245, vcc
	s_and_b32 s21, s77, 31
	s_lshl_b32 s21, 1, s21
	s_lshl_b32 s32, s21, 1
	v_and_b32_e32 v80, s21, v255
	v_cmp_ne_u32_e64 s[12:13], 0, v80
	v_and_b32_e32 v80, s32, v255
	v_cmp_ne_u32_e64 s[14:15], 0, v80
	s_nop 3
	s_or_b64 s[22:23], s[12:13], s[14:15]
	s_bcnt1_i32_b64 s11, s[22:23]
	s_add_i32 s11, s11, 3
	s_lshr_b32 s11, s11, 2
	s_cmp_ge_u32 s91, s11
	s_cbranch_scc1 .Lbm_g1_end_af
	s_add_i32 s83, s91, 8
	s_cmp_lt_u32 s83, s11
	s_cselect_b32 s83, 0x10000, 0
	s_add_i32 s83, s83, s75
	s_add_i32 s83, s83, 2
	s_andn2_b64 s[84:85], s[12:13], s[14:15]
	s_bcnt1_i32_b64 s77, s[84:85]
	v_mbcnt_lo_u32_b32 v80, s84, 0
	v_mbcnt_hi_u32_b32 v80, s85, v80
	v_mov_b32_e32 v255, s77
	s_and_b64 s[84:85], s[12:13], s[14:15]
	s_bcnt1_i32_b64 s32, s[84:85]
	v_mbcnt_lo_u32_b32 v255, s84, v255
	v_mbcnt_hi_u32_b32 v255, s85, v255
	s_add_i32 s77, s77, s32
	v_cndmask_b32_e64 v80, v80, v255, s[84:85]
	v_mov_b32_e32 v255, s77
	s_andn2_b64 s[84:85], s[14:15], s[12:13]
	v_mbcnt_lo_u32_b32 v255, s84, v255
	v_mbcnt_hi_u32_b32 v255, s85, v255
	s_nop 0
	v_cndmask_b32_e64 v80, v80, v255, s[84:85]
	v_cndmask_b32_e64 v78, 0, 1, s[12:13]
	v_cndmask_b32_e64 v255, 0, 2, s[14:15]
	v_or_b32_e32 v78, v78, v255
	v_and_b32_e32 v255, 63, v185
	v_lshl_or_b32 v78, v78, 6, v255
	s_lshl_b32 s77, s91, 6
	s_add_i32 s77, s77, 0x20900
	v_add_u32_e32 v255, s77, v80
	s_and_saveexec_b64 s[84:85], s[22:23]
	ds_write_b8 v255, v78
	s_mov_b64 exec, s[84:85]
	s_lshl_b32 s32, s91, 2
	s_bcnt1_i32_b64 s84, s[22:23]
	v_lshrrev_b32_e32 v78, 2, v250
	v_add_u32_e32 v78, s32, v78
	v_cmp_gt_u32_e32 vcc, s84, v78
	v_add_u32_e32 v255, s77, v78
	ds_read_u8 v251, v255
	v_cndmask_b32_e64 v254, -1, 0, vcc
.Lbm_g1_end_af:
	s_waitcnt lgkmcnt(10)
	v_mfma_f32_16x16x32_bf16 v[70:73], v[116:119], v[104:107], v[70:73]
	v_mov_b32_e32 v54, v82
	v_mov_b32_e32 v55, v82
	v_mfma_f32_16x16x32_bf16 v[70:73], v[120:123], v[108:111], v[70:73]
	v_mov_b32_e32 v56, v82
	v_mov_b32_e32 v57, v82
	s_waitcnt lgkmcnt(8)
	v_mfma_f32_16x16x32_bf16 v[74:77], v[124:127], v[104:107], v[74:77]
	v_mov_b32_e32 v58, v82
	v_mov_b32_e32 v59, v82
	v_mfma_f32_16x16x32_bf16 v[74:77], v[128:131], v[108:111], v[74:77]
	v_mov_b32_e32 v60, v82
	v_mov_b32_e32 v61, v82
	ds_read_b128 v[116:119], v148 offset:32768
	ds_read_b128 v[120:123], v149 offset:32768
	ds_read_b128 v[124:127], v148 offset:34816
	ds_read_b128 v[128:131], v149 offset:34816
	s_waitcnt lgkmcnt(10)
	v_mfma_f32_16x16x32_bf16 v[200:203], v[132:135], v[104:107], v[200:203]
	v_mov_b32_e32 v62, v82
	v_mov_b32_e32 v63, v82
	v_mfma_f32_16x16x32_bf16 v[200:203], v[136:139], v[108:111], v[200:203]
	v_mov_b32_e32 v64, v82
	v_mov_b32_e32 v65, v82
	s_waitcnt lgkmcnt(8)
	v_mfma_f32_16x16x32_bf16 v[204:207], v[140:143], v[104:107], v[204:207]
	v_mov_b32_e32 v66, v82
	v_mov_b32_e32 v67, v82
	v_mfma_f32_16x16x32_bf16 v[204:207], v[144:147], v[108:111], v[204:207]
	v_mov_b32_e32 v68, v82
	v_mov_b32_e32 v69, v82
	ds_read_b128 v[132:135], v148 offset:36864
	ds_read_b128 v[136:139], v149 offset:36864
	ds_read_b128 v[140:143], v148 offset:38912
	ds_read_b128 v[144:147], v149 offset:38912
	s_waitcnt lgkmcnt(10)
	v_mfma_f32_16x16x32_bf16 v[54:57], v[38:41], v[104:107], v[54:57]
	v_exp_f32_e32 v70, v70
	v_exp_f32_e32 v71, v71
	v_mfma_f32_16x16x32_bf16 v[54:57], v[42:45], v[108:111], v[54:57]
	v_exp_f32_e32 v72, v72
	v_exp_f32_e32 v73, v73
	s_waitcnt lgkmcnt(8)
	v_mfma_f32_16x16x32_bf16 v[58:61], v[46:49], v[104:107], v[58:61]
	v_exp_f32_e32 v74, v74
	v_exp_f32_e32 v75, v75
	v_mfma_f32_16x16x32_bf16 v[58:61], v[50:53], v[108:111], v[58:61]
	v_exp_f32_e32 v76, v76
	v_exp_f32_e32 v77, v77
	ds_read_b128 v[38:41], v208 offset:4096
	ds_read_b128 v[42:45], v209 offset:4096
	ds_read_b128 v[46:49], v208 offset:6144
	ds_read_b128 v[50:53], v209 offset:6144
	v_cvt_pk_bf16_f32 v70, v70, v71
	v_cvt_pk_bf16_f32 v71, v72, v73
	v_cvt_pk_bf16_f32 v72, v74, v75
	v_cvt_pk_bf16_f32 v73, v76, v77
	s_nop 1
	s_waitcnt lgkmcnt(4)
; __device__ __forceinline__ float ex2(float x) { return __builtin_amdgcn_exp2f(x); }
; template <bool SELMASK>
; __device__ __forceinline__ void attn_far_fast(const LAS unsigned char* kb, const LAS unsigned char* vb, const bf16x8 (&qf)[2][2], int col, int q, float bias_far, bool sel0, bool sel1, Softmax (&st)[2], f32x4 (&O)[2][4]) {
;     ...
;     bf16x8 pf[2][2];
; #pragma unroll
;     for (int c = 0; c < 2; ++c) {
;         const bool sel = c == 0 ? sel0 : sel1;
;         const float off = ((SELMASK && !sel) ? NEG : bias_far) - st[c].m;
; #pragma unroll
;         for (int kt = 0; kt < 4; ++kt) { f32x4 p = S[c][kt] + off;
; #pragma unroll
;             for (int e = 0; e < 4; ++e) p[e] = ex2(p[e]);
;             S[c][kt] = p; }
;         pf[c][0] = pack8(S[c][0], S[c][1]); pf[c][1] = pack8(S[c][2], S[c][3]);
;         st[c].l = __builtin_amdgcn_mfma_f32_16x16x32_bf16(ONES8, pf[c][0], st[c].l, 0, 0, 0); st[c].l = __builtin_amdgcn_mfma_f32_16x16x32_bf16(ONES8, pf[c][1], st[c].l, 0, 0, 0);
;     }
; #pragma unroll
;     for (int c32 = 0; c32 < 2; ++c32)
; #pragma unroll
;         for (int dt = 0; dt < 4; ++dt) { const bf16x8 vf = lds_frag(vb, 16 * dt + col, 4 * c32 + q);
;             O[0][dt] = __builtin_amdgcn_mfma_f32_16x16x32_bf16(vf, pf[0][c32], O[0][dt], 0, 0, 0);
;             O[1][dt] = __builtin_amdgcn_mfma_f32_16x16x32_bf16(vf, pf[1][c32], O[1][dt], 0, 0, 0); }
	v_mfma_f32_16x16x32_bf16 v[100:103], v[112:115], v[70:73], 0
	v_exp_f32_e32 v200, v200
	v_exp_f32_e32 v201, v201
	v_mfma_f32_16x16x32_bf16 v[84:87], v[116:119], v[70:73], 0
	v_exp_f32_e32 v202, v202
	v_exp_f32_e32 v203, v203
	v_mfma_f32_16x16x32_bf16 v[88:91], v[124:127], v[70:73], 0
	v_exp_f32_e32 v204, v204
	v_exp_f32_e32 v205, v205
	v_mfma_f32_16x16x32_bf16 v[92:95], v[132:135], v[70:73], 0
	v_exp_f32_e32 v206, v206
	v_exp_f32_e32 v207, v207
	v_mfma_f32_16x16x32_bf16 v[96:99], v[140:143], v[70:73], 0
	v_cvt_pk_bf16_f32 v74, v200, v201
	v_cvt_pk_bf16_f32 v75, v202, v203
	v_cvt_pk_bf16_f32 v76, v204, v205
	v_cvt_pk_bf16_f32 v77, v206, v207
	s_waitcnt lgkmcnt(2)
	v_mfma_f32_16x16x32_bf16 v[62:65], v[38:41], v[104:107], v[62:65]
	v_exp_f32_e32 v54, v54
	v_exp_f32_e32 v55, v55
	v_mfma_f32_16x16x32_bf16 v[62:65], v[42:45], v[108:111], v[62:65]
	v_exp_f32_e32 v56, v56
	v_exp_f32_e32 v57, v57
	s_waitcnt lgkmcnt(0)
	v_mfma_f32_16x16x32_bf16 v[66:69], v[46:49], v[104:107], v[66:69]
	v_exp_f32_e32 v58, v58
	v_exp_f32_e32 v59, v59
	v_mfma_f32_16x16x32_bf16 v[66:69], v[50:53], v[108:111], v[66:69]
	v_exp_f32_e32 v60, v60
	v_exp_f32_e32 v61, v61
	v_mfma_f32_16x16x32_bf16 v[100:103], v[112:115], v[74:77], v[100:103]
	v_cvt_pk_bf16_f32 v54, v54, v55
	v_mfma_f32_16x16x32_bf16 v[84:87], v[120:123], v[74:77], v[84:87]
	v_cvt_pk_bf16_f32 v55, v56, v57
	v_mfma_f32_16x16x32_bf16 v[88:91], v[128:131], v[74:77], v[88:91]
	v_cvt_pk_bf16_f32 v56, v58, v59
	v_mfma_f32_16x16x32_bf16 v[92:95], v[136:139], v[74:77], v[92:95]
	v_cvt_pk_bf16_f32 v57, v60, v61
	v_mfma_f32_16x16x32_bf16 v[96:99], v[144:147], v[74:77], v[96:99]
	ds_read_b128 v[116:119], v208 offset:32768
	ds_read_b128 v[120:123], v209 offset:32768
	ds_read_b128 v[124:127], v208 offset:34816
	ds_read_b128 v[128:131], v209 offset:34816
	ds_read_b128 v[132:135], v208 offset:36864
	ds_read_b128 v[136:139], v209 offset:36864
	ds_read_b128 v[140:143], v208 offset:38912
	ds_read_b128 v[144:147], v209 offset:38912
	s_mov_b32 s100, -1
	s_cmp_lt_i32 s83, 0
	s_cbranch_scc1 .Lbm_g2_end_af
	s_waitcnt lgkmcnt(8)
	v_or_b32_e32 v251, v251, v254
	v_max_i32_e32 v254, 0, v251
	v_and_b32_e32 v254, 63, v254
	v_lshlrev_b32_e32 v254, 11, v254
	v_mov_b32_e32 v255, 0
	v_lshl_add_u64 v[254:255], v[254:255], 0, v[246:247]
	global_load_dwordx4 v[104:107], v[254:255], off
	global_load_dwordx4 v[108:111], v[254:255], off offset:64
	s_mov_b32 s100, s83
.Lbm_g2_end_af:
	s_waitcnt lgkmcnt(0)
	v_mfma_f32_16x16x32_bf16 v[100:103], v[112:115], v[54:57], v[100:103]
	v_exp_f32_e32 v62, v62
	v_exp_f32_e32 v63, v63
	v_mfma_f32_16x16x32_bf16 v[84:87], v[116:119], v[54:57], v[84:87]
	v_exp_f32_e32 v64, v64
	v_exp_f32_e32 v65, v65
	v_mfma_f32_16x16x32_bf16 v[88:91], v[124:127], v[54:57], v[88:91]
	v_exp_f32_e32 v66, v66
	v_exp_f32_e32 v67, v67
	v_mfma_f32_16x16x32_bf16 v[92:95], v[132:135], v[54:57], v[92:95]
	v_exp_f32_e32 v68, v68
	v_exp_f32_e32 v69, v69
	v_mfma_f32_16x16x32_bf16 v[96:99], v[140:143], v[54:57], v[96:99]
	v_cvt_pk_bf16_f32 v58, v62, v63
	v_cvt_pk_bf16_f32 v59, v64, v65
	v_cvt_pk_bf16_f32 v60, v66, v67
	v_cvt_pk_bf16_f32 v61, v68, v69
	v_lshlrev_b32_e32 v254, 6, v186
	v_sub_u32_e32 v254, v83, v254
	ds_read2_b32 v[200:201], v83 offset0:0 offset1:4
	ds_read2_b32 v[202:203], v83 offset0:8 offset1:12
	ds_read2_b32 v[204:205], v83 offset0:64 offset1:68
	ds_read2_b32 v[206:207], v83 offset0:72 offset1:76
	ds_read2_b32 v[62:63], v83 offset0:128 offset1:132
	ds_read2_b32 v[64:65], v83 offset0:136 offset1:140
	ds_read2_b32 v[66:67], v83 offset0:192 offset1:196
	ds_read2_b32 v[68:69], v83 offset0:200 offset1:204
	ds_read_b32 v199, v254 offset:1024
	v_mfma_f32_16x16x32_bf16 v[100:103], v[112:115], v[58:61], v[100:103]
	v_mfma_f32_16x16x32_bf16 v[84:87], v[120:123], v[58:61], v[84:87]
	v_mfma_f32_16x16x32_bf16 v[88:91], v[128:131], v[58:61], v[88:91]
	v_mfma_f32_16x16x32_bf16 v[92:95], v[136:139], v[58:61], v[92:95]
	v_mfma_f32_16x16x32_bf16 v[96:99], v[144:147], v[58:61], v[96:99]
	s_nop 1
	s_waitcnt lgkmcnt(0)
	v_add_f32_e32 v200, v200, v84
	v_add_f32_e32 v201, v201, v85
	v_add_f32_e32 v202, v202, v86
	v_add_f32_e32 v203, v203, v87
	v_add_f32_e32 v204, v204, v88
	v_add_f32_e32 v205, v205, v89
	v_add_f32_e32 v206, v206, v90
	v_add_f32_e32 v207, v207, v91
	v_add_f32_e32 v199, v199, v100
	v_add_f32_e32 v62, v62, v92
	v_add_f32_e32 v63, v63, v93
	v_add_f32_e32 v64, v64, v94
	v_add_f32_e32 v65, v65, v95
	v_add_f32_e32 v66, v66, v96
	v_add_f32_e32 v67, v67, v97
	v_add_f32_e32 v68, v68, v98
	v_add_f32_e32 v69, v69, v99
	v_cmp_ne_u32_e32 vcc, 0, v79
	s_and_saveexec_b64 s[84:85], vcc
	ds_write2_b32 v83, v200, v201 offset0:0 offset1:4
	ds_write2_b32 v83, v202, v203 offset0:8 offset1:12
	ds_write2_b32 v83, v204, v205 offset0:64 offset1:68
	ds_write2_b32 v83, v206, v207 offset0:72 offset1:76
	ds_write2_b32 v83, v62, v63 offset0:128 offset1:132
	ds_write2_b32 v83, v64, v65 offset0:136 offset1:140
	ds_write2_b32 v83, v66, v67 offset0:192 offset1:196
	ds_write2_b32 v83, v68, v69 offset0:200 offset1:204
	ds_write_b32 v254, v199 offset:1024
	s_mov_b64 exec, s[84:85]
	s_nop 3
	s_branch .Lbm_done

; __device__ __forceinline__ float ex2(float x) { return __builtin_amdgcn_exp2f(x); }
; template <bool SELMASK>
; __device__ __forceinline__ void attn_far_fast(const LAS unsigned char* kb, const LAS unsigned char* vb, const bf16x8 (&qf)[2][2], int col, int q, float bias_far, bool sel0, bool sel1, Softmax (&st)[2], f32x4 (&O)[2][4]) {
;     ...
;     f32x4 S[2][4];
; #pragma unroll
;     for (int kt = 0; kt < 4; ++kt) { const bf16x8 k0 = lds_frag(kb, 16 * kt + col, q), k1 = lds_frag(kb, 16 * kt + col, 4 + q);
; #pragma unroll
;         for (int c = 0; c < 2; ++c) { S[c][kt] = __builtin_amdgcn_mfma_f32_16x16x32_bf16(k0, qf[c][0], z4, 0, 0, 0); S[c][kt] = __builtin_amdgcn_mfma_f32_16x16x32_bf16(k1, qf[c][1], S[c][kt], 0, 0, 0); } }
;     bf16x8 pf[2][2];
; #pragma unroll
;     for (int c = 0; c < 2; ++c) {
;         const bool sel = c == 0 ? sel0 : sel1;
;         const float off = ((SELMASK && !sel) ? NEG : bias_far) - st[c].m;
; #pragma unroll
;         for (int kt = 0; kt < 4; ++kt) { f32x4 p = S[c][kt] + off;
; #pragma unroll
;             for (int e = 0; e < 4; ++e) p[e] = ex2(p[e]);
;             S[c][kt] = p; }
;         pf[c][0] = pack8(S[c][0], S[c][1]); pf[c][1] = pack8(S[c][2], S[c][3]);
;         st[c].l = __builtin_amdgcn_mfma_f32_16x16x32_bf16(ONES8, pf[c][0], st[c].l, 0, 0, 0); st[c].l = __builtin_amdgcn_mfma_f32_16x16x32_bf16(ONES8, pf[c][1], st[c].l, 0, 0, 0);
;     }
; #pragma unroll
;     for (int c32 = 0; c32 < 2; ++c32)
; #pragma unroll
;         for (int dt = 0; dt < 4; ++dt) { const bf16x8 vf = lds_frag(vb, 16 * dt + col, 4 * c32 + q);
;             O[0][dt] = __builtin_amdgcn_mfma_f32_16x16x32_bf16(vf, pf[0][c32], O[0][dt], 0, 0, 0);
;             O[1][dt] = __builtin_amdgcn_mfma_f32_16x16x32_bf16(vf, pf[1][c32], O[1][dt], 0, 0, 0); }
.Lbm_r1_two:
	v_add_u32_e32 v148, s83, v192
	v_add_u32_e32 v149, v148, v195
	v_add_u32_e32 v148, v148, v193
	ds_read_b128 v[116:119], v148
	ds_read_b128 v[120:123], v149
	ds_read_b128 v[124:127], v148 offset:2048
	ds_read_b128 v[128:131], v149 offset:2048
	ds_read_b128 v[132:135], v148 offset:4096
	ds_read_b128 v[136:139], v149 offset:4096
	ds_read_b128 v[140:143], v148 offset:6144
	ds_read_b128 v[144:147], v149 offset:6144
	s_add_i32 s32, s1, 0x2000
	s_and_b32 s32, s32, 0x6000
	v_add_u32_e32 v208, s32, v192
	v_add_u32_e32 v209, v208, v195
	v_add_u32_e32 v208, v208, v193
	ds_read_b128 v[38:41], v208
	ds_read_b128 v[42:45], v209
	ds_read_b128 v[46:49], v208 offset:2048
	ds_read_b128 v[50:53], v209 offset:2048
	s_waitcnt lgkmcnt(12)
	v_sub_f32_e32 v81, v81, v199
	v_sub_f32_e32 v82, v82, v199
	v_mov_b32_e32 v70, v81
	v_mov_b32_e32 v71, v81
	v_mov_b32_e32 v72, v81
	v_mov_b32_e32 v73, v81
	v_mov_b32_e32 v74, v81
	v_mov_b32_e32 v75, v81
	v_mov_b32_e32 v76, v81
	v_mov_b32_e32 v77, v81
	v_mov_b32_e32 v200, v81
	v_mov_b32_e32 v201, v81
	v_mov_b32_e32 v202, v81
	v_mov_b32_e32 v203, v81
	v_mov_b32_e32 v204, v81
	v_mov_b32_e32 v205, v81
	v_mov_b32_e32 v206, v81
	v_mov_b32_e32 v207, v81
	s_waitcnt lgkmcnt(10)
	v_mfma_f32_16x16x32_bf16 v[70:73], v[116:119], v[104:107], v[70:73]
	v_mov_b32_e32 v54, v82
	v_mov_b32_e32 v55, v82
	v_mfma_f32_16x16x32_bf16 v[70:73], v[120:123], v[108:111], v[70:73]
	v_mov_b32_e32 v56, v82
	v_mov_b32_e32 v57, v82
	s_waitcnt lgkmcnt(8)
	v_mfma_f32_16x16x32_bf16 v[74:77], v[124:127], v[104:107], v[74:77]
	v_mov_b32_e32 v58, v82
	v_mov_b32_e32 v59, v82
	v_mfma_f32_16x16x32_bf16 v[74:77], v[128:131], v[108:111], v[74:77]
	v_mov_b32_e32 v60, v82
	v_mov_b32_e32 v61, v82
	ds_read_b128 v[116:119], v148 offset:32768
	ds_read_b128 v[120:123], v149 offset:32768
	ds_read_b128 v[124:127], v148 offset:34816
	ds_read_b128 v[128:131], v149 offset:34816
	s_waitcnt lgkmcnt(10)
	v_mfma_f32_16x16x32_bf16 v[200:203], v[132:135], v[104:107], v[200:203]
	v_mov_b32_e32 v62, v82
	v_mov_b32_e32 v63, v82
	v_mfma_f32_16x16x32_bf16 v[200:203], v[136:139], v[108:111], v[200:203]
	v_mov_b32_e32 v64, v82
	v_mov_b32_e32 v65, v82
	s_waitcnt lgkmcnt(8)
	v_mfma_f32_16x16x32_bf16 v[204:207], v[140:143], v[104:107], v[204:207]
	v_mov_b32_e32 v66, v82
	v_mov_b32_e32 v67, v82
	v_mfma_f32_16x16x32_bf16 v[204:207], v[144:147], v[108:111], v[204:207]
	v_mov_b32_e32 v68, v82
	v_mov_b32_e32 v69, v82
	ds_read_b128 v[132:135], v148 offset:36864
	ds_read_b128 v[136:139], v149 offset:36864
	ds_read_b128 v[140:143], v148 offset:38912
	ds_read_b128 v[144:147], v149 offset:38912
	s_waitcnt lgkmcnt(10)
	v_mfma_f32_16x16x32_bf16 v[54:57], v[38:41], v[104:107], v[54:57]
	v_exp_f32_e32 v70, v70
	v_exp_f32_e32 v71, v71
	v_mfma_f32_16x16x32_bf16 v[54:57], v[42:45], v[108:111], v[54:57]
	v_exp_f32_e32 v72, v72
	v_exp_f32_e32 v73, v73
	s_waitcnt lgkmcnt(8)
	v_mfma_f32_16x16x32_bf16 v[58:61], v[46:49], v[104:107], v[58:61]
	v_exp_f32_e32 v74, v74
	v_exp_f32_e32 v75, v75
	v_mfma_f32_16x16x32_bf16 v[58:61], v[50:53], v[108:111], v[58:61]
	v_exp_f32_e32 v76, v76
	v_exp_f32_e32 v77, v77
	ds_read_b128 v[38:41], v208 offset:4096
	ds_read_b128 v[42:45], v209 offset:4096
	ds_read_b128 v[46:49], v208 offset:6144
	ds_read_b128 v[50:53], v209 offset:6144
	v_cvt_pk_bf16_f32 v70, v70, v71
	v_cvt_pk_bf16_f32 v71, v72, v73
	v_cvt_pk_bf16_f32 v72, v74, v75
	v_cvt_pk_bf16_f32 v73, v76, v77
	s_nop 1
	s_waitcnt lgkmcnt(4)
	v_mfma_f32_16x16x32_bf16 v[100:103], v[112:115], v[70:73], 0
	v_exp_f32_e32 v200, v200
	v_exp_f32_e32 v201, v201
	v_mfma_f32_16x16x32_bf16 v[84:87], v[116:119], v[70:73], 0
	v_exp_f32_e32 v202, v202
	v_exp_f32_e32 v203, v203
	v_mfma_f32_16x16x32_bf16 v[88:91], v[124:127], v[70:73], 0
	v_exp_f32_e32 v204, v204
	v_exp_f32_e32 v205, v205
	v_mfma_f32_16x16x32_bf16 v[92:95], v[132:135], v[70:73], 0
	v_exp_f32_e32 v206, v206
	v_exp_f32_e32 v207, v207
	v_mfma_f32_16x16x32_bf16 v[96:99], v[140:143], v[70:73], 0
	v_cvt_pk_bf16_f32 v74, v200, v201
	v_cvt_pk_bf16_f32 v75, v202, v203
	v_cvt_pk_bf16_f32 v76, v204, v205
	v_cvt_pk_bf16_f32 v77, v206, v207
	s_waitcnt lgkmcnt(2)
	v_mfma_f32_16x16x32_bf16 v[62:65], v[38:41], v[104:107], v[62:65]
	v_exp_f32_e32 v54, v54
	v_exp_f32_e32 v55, v55
	v_mfma_f32_16x16x32_bf16 v[62:65], v[42:45], v[108:111], v[62:65]
	v_exp_f32_e32 v56, v56
	v_exp_f32_e32 v57, v57
	s_waitcnt lgkmcnt(0)
	v_mfma_f32_16x16x32_bf16 v[66:69], v[46:49], v[104:107], v[66:69]
	v_exp_f32_e32 v58, v58
	v_exp_f32_e32 v59, v59
	v_mfma_f32_16x16x32_bf16 v[66:69], v[50:53], v[108:111], v[66:69]
	v_exp_f32_e32 v60, v60
	v_exp_f32_e32 v61, v61
	v_mfma_f32_16x16x32_bf16 v[100:103], v[112:115], v[74:77], v[100:103]
	v_cvt_pk_bf16_f32 v54, v54, v55
	v_mfma_f32_16x16x32_bf16 v[84:87], v[120:123], v[74:77], v[84:87]
	v_cvt_pk_bf16_f32 v55, v56, v57
	v_mfma_f32_16x16x32_bf16 v[88:91], v[128:131], v[74:77], v[88:91]
	v_cvt_pk_bf16_f32 v56, v58, v59
	v_mfma_f32_16x16x32_bf16 v[92:95], v[136:139], v[74:77], v[92:95]
	v_cvt_pk_bf16_f32 v57, v60, v61
	v_mfma_f32_16x16x32_bf16 v[96:99], v[144:147], v[74:77], v[96:99]
	ds_read_b128 v[116:119], v208 offset:32768
	ds_read_b128 v[120:123], v209 offset:32768
	ds_read_b128 v[124:127], v208 offset:34816
	ds_read_b128 v[128:131], v209 offset:34816
	ds_read_b128 v[132:135], v208 offset:36864
	ds_read_b128 v[136:139], v209 offset:36864
	ds_read_b128 v[140:143], v208 offset:38912
	ds_read_b128 v[144:147], v209 offset:38912
	s_nop 3
	s_waitcnt lgkmcnt(0)
; __device__ __forceinline__ float ex2(float x) { return __builtin_amdgcn_exp2f(x); }
; template <bool SELMASK>
; __device__ __forceinline__ void attn_far_fast(const LAS unsigned char* kb, const LAS unsigned char* vb, const bf16x8 (&qf)[2][2], int col, int q, float bias_far, bool sel0, bool sel1, Softmax (&st)[2], f32x4 (&O)[2][4]) {
;     ...
;         for (int kt = 0; kt < 4; ++kt) { f32x4 p = S[c][kt] + off;
; #pragma unroll
;             for (int e = 0; e < 4; ++e) p[e] = ex2(p[e]);
;             S[c][kt] = p; }
;         pf[c][0] = pack8(S[c][0], S[c][1]); pf[c][1] = pack8(S[c][2], S[c][3]);
;         st[c].l = __builtin_amdgcn_mfma_f32_16x16x32_bf16(ONES8, pf[c][0], st[c].l, 0, 0, 0); st[c].l = __builtin_amdgcn_mfma_f32_16x16x32_bf16(ONES8, pf[c][1], st[c].l, 0, 0, 0);
;     }
; #pragma unroll
;     for (int c32 = 0; c32 < 2; ++c32)
; #pragma unroll
;         for (int dt = 0; dt < 4; ++dt) { const bf16x8 vf = lds_frag(vb, 16 * dt + col, 4 * c32 + q);
;             O[0][dt] = __builtin_amdgcn_mfma_f32_16x16x32_bf16(vf, pf[0][c32], O[0][dt], 0, 0, 0);
;             O[1][dt] = __builtin_amdgcn_mfma_f32_16x16x32_bf16(vf, pf[1][c32], O[1][dt], 0, 0, 0); }
	v_mfma_f32_16x16x32_bf16 v[100:103], v[112:115], v[54:57], v[100:103]
	v_exp_f32_e32 v62, v62
	v_exp_f32_e32 v63, v63
	v_mfma_f32_16x16x32_bf16 v[84:87], v[116:119], v[54:57], v[84:87]
	v_exp_f32_e32 v64, v64
	v_exp_f32_e32 v65, v65
	v_mfma_f32_16x16x32_bf16 v[88:91], v[124:127], v[54:57], v[88:91]
	v_exp_f32_e32 v66, v66
	v_exp_f32_e32 v67, v67
	v_mfma_f32_16x16x32_bf16 v[92:95], v[132:135], v[54:57], v[92:95]
	v_exp_f32_e32 v68, v68
	v_exp_f32_e32 v69, v69
	v_mfma_f32_16x16x32_bf16 v[96:99], v[140:143], v[54:57], v[96:99]
	v_cvt_pk_bf16_f32 v58, v62, v63
	v_cvt_pk_bf16_f32 v59, v64, v65
	v_cvt_pk_bf16_f32 v60, v66, v67
	v_cvt_pk_bf16_f32 v61, v68, v69
	v_lshlrev_b32_e32 v254, 6, v186
	v_sub_u32_e32 v254, v83, v254
	ds_read2_b32 v[200:201], v83 offset0:0 offset1:4
	ds_read2_b32 v[202:203], v83 offset0:8 offset1:12
	ds_read2_b32 v[204:205], v83 offset0:64 offset1:68
	ds_read2_b32 v[206:207], v83 offset0:72 offset1:76
	ds_read2_b32 v[62:63], v83 offset0:128 offset1:132
	ds_read2_b32 v[64:65], v83 offset0:136 offset1:140
	ds_read2_b32 v[66:67], v83 offset0:192 offset1:196
	ds_read2_b32 v[68:69], v83 offset0:200 offset1:204
	ds_read_b32 v199, v254 offset:1024
	v_mfma_f32_16x16x32_bf16 v[100:103], v[112:115], v[58:61], v[100:103]
	v_mfma_f32_16x16x32_bf16 v[84:87], v[120:123], v[58:61], v[84:87]
	v_mfma_f32_16x16x32_bf16 v[88:91], v[128:131], v[58:61], v[88:91]
	v_mfma_f32_16x16x32_bf16 v[92:95], v[136:139], v[58:61], v[92:95]
	v_mfma_f32_16x16x32_bf16 v[96:99], v[144:147], v[58:61], v[96:99]
	s_nop 1
	s_waitcnt lgkmcnt(0)
	v_add_f32_e32 v200, v200, v84
	v_add_f32_e32 v201, v201, v85
	v_add_f32_e32 v202, v202, v86
	v_add_f32_e32 v203, v203, v87
	v_add_f32_e32 v204, v204, v88
	v_add_f32_e32 v205, v205, v89
	v_add_f32_e32 v206, v206, v90
	v_add_f32_e32 v207, v207, v91
	v_add_f32_e32 v199, v199, v100
	v_add_f32_e32 v62, v62, v92
	v_add_f32_e32 v63, v63, v93
	v_add_f32_e32 v64, v64, v94
	v_add_f32_e32 v65, v65, v95
	v_add_f32_e32 v66, v66, v96
	v_add_f32_e32 v67, v67, v97
	v_add_f32_e32 v68, v68, v98
	v_add_f32_e32 v69, v69, v99
	v_cmp_ne_u32_e32 vcc, 0, v79
	s_and_saveexec_b64 s[84:85], vcc
	ds_write2_b32 v83, v200, v201 offset0:0 offset1:4
	ds_write2_b32 v83, v202, v203 offset0:8 offset1:12
	ds_write2_b32 v83, v204, v205 offset0:64 offset1:68
	ds_write2_b32 v83, v206, v207 offset0:72 offset1:76
	ds_write2_b32 v83, v62, v63 offset0:128 offset1:132
	ds_write2_b32 v83, v64, v65 offset0:136 offset1:140
	ds_write2_b32 v83, v66, v67 offset0:192 offset1:196
	ds_write2_b32 v83, v68, v69 offset0:200 offset1:204
	ds_write_b32 v254, v199 offset:1024
	s_mov_b64 exec, s[84:85]
	s_nop 3
	s_mov_b32 s100, -1
	s_add_i32 s21, s91, 8
	s_andn2_b64 s[84:85], s[12:13], s[14:15]
	s_bcnt1_i32_b64 s77, s[84:85]
	v_mbcnt_lo_u32_b32 v80, s84, 0
	v_mbcnt_hi_u32_b32 v80, s85, v80
	v_mov_b32_e32 v56, s77
	s_and_b64 s[84:85], s[12:13], s[14:15]
	s_bcnt1_i32_b64 s32, s[84:85]
	v_mbcnt_lo_u32_b32 v56, s84, v56
	v_mbcnt_hi_u32_b32 v56, s85, v56
	s_add_i32 s77, s77, s32
	v_cndmask_b32_e64 v80, v80, v56, s[84:85]
	v_mov_b32_e32 v56, s77
	s_andn2_b64 s[84:85], s[14:15], s[12:13]
	v_mbcnt_lo_u32_b32 v56, s84, v56
	v_mbcnt_hi_u32_b32 v56, s85, v56
	s_nop 0
	v_cndmask_b32_e64 v80, v80, v56, s[84:85]
	v_cndmask_b32_e64 v58, 0, 1, s[12:13]
	v_cndmask_b32_e64 v59, 0, 2, s[14:15]
	v_or_b32_e32 v58, v58, v59
	v_and_b32_e32 v59, 63, v185
	v_lshl_or_b32 v58, v58, 6, v59
	s_lshl_b32 s77, s91, 6
	s_add_i32 s77, s77, 0x20900
	v_add_u32_e32 v59, s77, v80
	s_and_saveexec_b64 s[84:85], s[22:23]
	ds_write_b8 v59, v58
	s_mov_b64 exec, s[84:85]
	s_lshl_b32 s32, s21, 2
	s_bcnt1_i32_b64 s84, s[22:23]
	v_lshrrev_b32_e32 v58, 2, v250
	v_add_u32_e32 v58, s32, v58
	v_cmp_gt_u32_e32 vcc, s84, v58
	v_add_u32_e32 v59, s77, v58
	ds_read_u8 v63, v59
	v_cndmask_b32_e64 v60, -1, 0, vcc
	s_waitcnt lgkmcnt(0)
	v_or_b32_e32 v63, v63, v60
	v_lshrrev_b32_e32 v56, 31, v63
	v_xor_b32_e32 v56, 1, v56
	v_max_i32_e32 v55, 0, v63
	v_mov_b32_e32 v79, v56
	v_and_b32_e32 v54, 63, v55
	v_bfe_u32 v58, v55, 6, 1
	v_bfe_u32 v59, v55, 7, 1
	v_lshlrev_b32_e32 v60, 11, v54
	v_mov_b32_e32 v61, 0
	v_lshl_add_u64 v[60:61], v[60:61], 0, v[246:247]
	global_load_dwordx4 v[104:107], v[60:61], off
	global_load_dwordx4 v[108:111], v[60:61], off offset:64
	v_lshl_add_u32 v63, v54, 4, v249
	ds_read_b32 v199, v63
	v_mul_u32_u24_e32 v83, 0x410, v54
	v_cmp_ne_u32_e32 vcc, 0, v58
	v_add_u32_e32 v83, v83, v248
	s_nop 0
	v_cndmask_b32_e32 v81, v2, v154, vcc
	s_cmp_lg_u64 vcc, 0
	s_cselect_b32 s21, 1, 0
	v_cmp_ne_u32_e32 vcc, 0, v59
	s_nop 1
	v_cndmask_b32_e32 v82, v2, v154, vcc
	s_cmp_lg_u64 vcc, 0
	s_cselect_b32 s32, 1, 0
	s_waitcnt vmcnt(0)
	s_and_b32 s83, s1, 0x4000
	v_add_u32_e32 v148, s83, v192
	v_add_u32_e32 v149, v148, v195
	v_add_u32_e32 v148, v148, v193
	ds_read_b128 v[116:119], v148
	ds_read_b128 v[120:123], v149
	ds_read_b128 v[124:127], v148 offset:2048
	ds_read_b128 v[128:131], v149 offset:2048
	ds_read_b128 v[132:135], v148 offset:4096
	ds_read_b128 v[136:139], v149 offset:4096
	ds_read_b128 v[140:143], v148 offset:6144
	ds_read_b128 v[144:147], v149 offset:6144
	s_add_i32 s32, s1, 0x2000
	s_and_b32 s32, s32, 0x6000
	v_add_u32_e32 v208, s32, v192
	v_add_u32_e32 v209, v208, v195
	v_add_u32_e32 v208, v208, v193
	ds_read_b128 v[38:41], v208
	ds_read_b128 v[42:45], v209
	ds_read_b128 v[46:49], v208 offset:2048
	ds_read_b128 v[50:53], v209 offset:2048
	s_waitcnt lgkmcnt(12)
	v_sub_f32_e32 v81, v81, v199
	v_sub_f32_e32 v82, v82, v199
	v_mov_b32_e32 v70, v81
	v_mov_b32_e32 v71, v81
	v_mov_b32_e32 v72, v81
	v_mov_b32_e32 v73, v81
	v_mov_b32_e32 v74, v81
	v_mov_b32_e32 v75, v81
	v_mov_b32_e32 v76, v81
	v_mov_b32_e32 v77, v81
	v_mov_b32_e32 v200, v81
	v_mov_b32_e32 v201, v81
	v_mov_b32_e32 v202, v81
	v_mov_b32_e32 v203, v81
	v_mov_b32_e32 v204, v81
	v_mov_b32_e32 v205, v81
	v_mov_b32_e32 v206, v81
	v_mov_b32_e32 v207, v81
	s_waitcnt lgkmcnt(10)
; __device__ __forceinline__ float ex2(float x) { return __builtin_amdgcn_exp2f(x); }
; template <bool SELMASK>
; __device__ __forceinline__ void attn_far_fast(const LAS unsigned char* kb, const LAS unsigned char* vb, const bf16x8 (&qf)[2][2], int col, int q, float bias_far, bool sel0, bool sel1, Softmax (&st)[2], f32x4 (&O)[2][4]) {
;     ...
;     f32x4 S[2][4];
; #pragma unroll
;     for (int kt = 0; kt < 4; ++kt) { const bf16x8 k0 = lds_frag(kb, 16 * kt + col, q), k1 = lds_frag(kb, 16 * kt + col, 4 + q);
; #pragma unroll
;         for (int c = 0; c < 2; ++c) { S[c][kt] = __builtin_amdgcn_mfma_f32_16x16x32_bf16(k0, qf[c][0], z4, 0, 0, 0); S[c][kt] = __builtin_amdgcn_mfma_f32_16x16x32_bf16(k1, qf[c][1], S[c][kt], 0, 0, 0); } }
;     bf16x8 pf[2][2];
; #pragma unroll
;     for (int c = 0; c < 2; ++c) {
;         const bool sel = c == 0 ? sel0 : sel1;
;         const float off = ((SELMASK && !sel) ? NEG : bias_far) - st[c].m;
; #pragma unroll
;         for (int kt = 0; kt < 4; ++kt) { f32x4 p = S[c][kt] + off;
; #pragma unroll
;             for (int e = 0; e < 4; ++e) p[e] = ex2(p[e]);
;             S[c][kt] = p; }
;         pf[c][0] = pack8(S[c][0], S[c][1]); pf[c][1] = pack8(S[c][2], S[c][3]);
;         st[c].l = __builtin_amdgcn_mfma_f32_16x16x32_bf16(ONES8, pf[c][0], st[c].l, 0, 0, 0); st[c].l = __builtin_amdgcn_mfma_f32_16x16x32_bf16(ONES8, pf[c][1], st[c].l, 0, 0, 0);
;     }
; #pragma unroll
;     for (int c32 = 0; c32 < 2; ++c32)
; #pragma unroll
;         for (int dt = 0; dt < 4; ++dt) { const bf16x8 vf = lds_frag(vb, 16 * dt + col, 4 * c32 + q);
;             O[0][dt] = __builtin_amdgcn_mfma_f32_16x16x32_bf16(vf, pf[0][c32], O[0][dt], 0, 0, 0);
;             O[1][dt] = __builtin_amdgcn_mfma_f32_16x16x32_bf16(vf, pf[1][c32], O[1][dt], 0, 0, 0); }
	v_mfma_f32_16x16x32_bf16 v[70:73], v[116:119], v[104:107], v[70:73]
	v_mov_b32_e32 v54, v82
	v_mov_b32_e32 v55, v82
	v_mfma_f32_16x16x32_bf16 v[70:73], v[120:123], v[108:111], v[70:73]
	v_mov_b32_e32 v56, v82
	v_mov_b32_e32 v57, v82
	s_waitcnt lgkmcnt(8)
	v_mfma_f32_16x16x32_bf16 v[74:77], v[124:127], v[104:107], v[74:77]
	v_mov_b32_e32 v58, v82
	v_mov_b32_e32 v59, v82
	v_mfma_f32_16x16x32_bf16 v[74:77], v[128:131], v[108:111], v[74:77]
	v_mov_b32_e32 v60, v82
	v_mov_b32_e32 v61, v82
	ds_read_b128 v[116:119], v148 offset:32768
	ds_read_b128 v[120:123], v149 offset:32768
	ds_read_b128 v[124:127], v148 offset:34816
	ds_read_b128 v[128:131], v149 offset:34816
	s_waitcnt lgkmcnt(10)
	v_mfma_f32_16x16x32_bf16 v[200:203], v[132:135], v[104:107], v[200:203]
	v_mov_b32_e32 v62, v82
	v_mov_b32_e32 v63, v82
	v_mfma_f32_16x16x32_bf16 v[200:203], v[136:139], v[108:111], v[200:203]
	v_mov_b32_e32 v64, v82
	v_mov_b32_e32 v65, v82
	s_waitcnt lgkmcnt(8)
	v_mfma_f32_16x16x32_bf16 v[204:207], v[140:143], v[104:107], v[204:207]
	v_mov_b32_e32 v66, v82
	v_mov_b32_e32 v67, v82
	v_mfma_f32_16x16x32_bf16 v[204:207], v[144:147], v[108:111], v[204:207]
	v_mov_b32_e32 v68, v82
	v_mov_b32_e32 v69, v82
	ds_read_b128 v[132:135], v148 offset:36864
	ds_read_b128 v[136:139], v149 offset:36864
	ds_read_b128 v[140:143], v148 offset:38912
	ds_read_b128 v[144:147], v149 offset:38912
	s_waitcnt lgkmcnt(10)
	v_mfma_f32_16x16x32_bf16 v[54:57], v[38:41], v[104:107], v[54:57]
	v_exp_f32_e32 v70, v70
	v_exp_f32_e32 v71, v71
	v_mfma_f32_16x16x32_bf16 v[54:57], v[42:45], v[108:111], v[54:57]
	v_exp_f32_e32 v72, v72
	v_exp_f32_e32 v73, v73
	s_waitcnt lgkmcnt(8)
	v_mfma_f32_16x16x32_bf16 v[58:61], v[46:49], v[104:107], v[58:61]
	v_exp_f32_e32 v74, v74
	v_exp_f32_e32 v75, v75
	v_mfma_f32_16x16x32_bf16 v[58:61], v[50:53], v[108:111], v[58:61]
	v_exp_f32_e32 v76, v76
	v_exp_f32_e32 v77, v77
	ds_read_b128 v[38:41], v208 offset:4096
	ds_read_b128 v[42:45], v209 offset:4096
	ds_read_b128 v[46:49], v208 offset:6144
	ds_read_b128 v[50:53], v209 offset:6144
	v_cvt_pk_bf16_f32 v70, v70, v71
	v_cvt_pk_bf16_f32 v71, v72, v73
	v_cvt_pk_bf16_f32 v72, v74, v75
	v_cvt_pk_bf16_f32 v73, v76, v77
	s_nop 1
	s_waitcnt lgkmcnt(4)
	v_mfma_f32_16x16x32_bf16 v[100:103], v[112:115], v[70:73], 0
	v_exp_f32_e32 v200, v200
	v_exp_f32_e32 v201, v201
	v_mfma_f32_16x16x32_bf16 v[84:87], v[116:119], v[70:73], 0
	v_exp_f32_e32 v202, v202
	v_exp_f32_e32 v203, v203
	v_mfma_f32_16x16x32_bf16 v[88:91], v[124:127], v[70:73], 0
	v_exp_f32_e32 v204, v204
	v_exp_f32_e32 v205, v205
	v_mfma_f32_16x16x32_bf16 v[92:95], v[132:135], v[70:73], 0
	v_exp_f32_e32 v206, v206
	v_exp_f32_e32 v207, v207
	v_mfma_f32_16x16x32_bf16 v[96:99], v[140:143], v[70:73], 0
	v_cvt_pk_bf16_f32 v74, v200, v201
	v_cvt_pk_bf16_f32 v75, v202, v203
	v_cvt_pk_bf16_f32 v76, v204, v205
	v_cvt_pk_bf16_f32 v77, v206, v207
	s_waitcnt lgkmcnt(2)
	v_mfma_f32_16x16x32_bf16 v[62:65], v[38:41], v[104:107], v[62:65]
	v_exp_f32_e32 v54, v54
	v_exp_f32_e32 v55, v55
	v_mfma_f32_16x16x32_bf16 v[62:65], v[42:45], v[108:111], v[62:65]
	v_exp_f32_e32 v56, v56
	v_exp_f32_e32 v57, v57
	s_waitcnt lgkmcnt(0)
	v_mfma_f32_16x16x32_bf16 v[66:69], v[46:49], v[104:107], v[66:69]
	v_exp_f32_e32 v58, v58
	v_exp_f32_e32 v59, v59
	v_mfma_f32_16x16x32_bf16 v[66:69], v[50:53], v[108:111], v[66:69]
	v_exp_f32_e32 v60, v60
	v_exp_f32_e32 v61, v61
	v_mfma_f32_16x16x32_bf16 v[100:103], v[112:115], v[74:77], v[100:103]
	v_cvt_pk_bf16_f32 v54, v54, v55
	v_mfma_f32_16x16x32_bf16 v[84:87], v[120:123], v[74:77], v[84:87]
	v_cvt_pk_bf16_f32 v55, v56, v57
	v_mfma_f32_16x16x32_bf16 v[88:91], v[128:131], v[74:77], v[88:91]
	v_cvt_pk_bf16_f32 v56, v58, v59
	v_mfma_f32_16x16x32_bf16 v[92:95], v[136:139], v[74:77], v[92:95]
	v_cvt_pk_bf16_f32 v57, v60, v61
	v_mfma_f32_16x16x32_bf16 v[96:99], v[144:147], v[74:77], v[96:99]
	ds_read_b128 v[116:119], v208 offset:32768
	ds_read_b128 v[120:123], v209 offset:32768
	ds_read_b128 v[124:127], v208 offset:34816
	ds_read_b128 v[128:131], v209 offset:34816
	ds_read_b128 v[132:135], v208 offset:36864
	ds_read_b128 v[136:139], v209 offset:36864
	ds_read_b128 v[140:143], v208 offset:38912
	ds_read_b128 v[144:147], v209 offset:38912
	s_nop 3
	s_waitcnt lgkmcnt(0)
	v_mfma_f32_16x16x32_bf16 v[100:103], v[112:115], v[54:57], v[100:103]
	v_exp_f32_e32 v62, v62
	v_exp_f32_e32 v63, v63
	v_mfma_f32_16x16x32_bf16 v[84:87], v[116:119], v[54:57], v[84:87]
	v_exp_f32_e32 v64, v64
	v_exp_f32_e32 v65, v65
	v_mfma_f32_16x16x32_bf16 v[88:91], v[124:127], v[54:57], v[88:91]
	v_exp_f32_e32 v66, v66
	v_exp_f32_e32 v67, v67
	v_mfma_f32_16x16x32_bf16 v[92:95], v[132:135], v[54:57], v[92:95]
	v_exp_f32_e32 v68, v68
	v_exp_f32_e32 v69, v69
	v_mfma_f32_16x16x32_bf16 v[96:99], v[140:143], v[54:57], v[96:99]
	v_cvt_pk_bf16_f32 v58, v62, v63
	v_cvt_pk_bf16_f32 v59, v64, v65
	v_cvt_pk_bf16_f32 v60, v66, v67
	v_cvt_pk_bf16_f32 v61, v68, v69
	v_lshlrev_b32_e32 v254, 6, v186
	v_sub_u32_e32 v254, v83, v254
	ds_read2_b32 v[200:201], v83 offset0:0 offset1:4
	ds_read2_b32 v[202:203], v83 offset0:8 offset1:12
	ds_read2_b32 v[204:205], v83 offset0:64 offset1:68
	ds_read2_b32 v[206:207], v83 offset0:72 offset1:76
	ds_read2_b32 v[62:63], v83 offset0:128 offset1:132
	ds_read2_b32 v[64:65], v83 offset0:136 offset1:140
	ds_read2_b32 v[66:67], v83 offset0:192 offset1:196
	ds_read2_b32 v[68:69], v83 offset0:200 offset1:204
	ds_read_b32 v199, v254 offset:1024
	v_mfma_f32_16x16x32_bf16 v[100:103], v[112:115], v[58:61], v[100:103]
	v_mfma_f32_16x16x32_bf16 v[84:87], v[120:123], v[58:61], v[84:87]
	v_mfma_f32_16x16x32_bf16 v[88:91], v[128:131], v[58:61], v[88:91]
	v_mfma_f32_16x16x32_bf16 v[92:95], v[136:139], v[58:61], v[92:95]
	v_mfma_f32_16x16x32_bf16 v[96:99], v[144:147], v[58:61], v[96:99]
	s_nop 1
	s_waitcnt lgkmcnt(0)
	v_add_f32_e32 v200, v200, v84
	v_add_f32_e32 v201, v201, v85
	v_add_f32_e32 v202, v202, v86
	v_add_f32_e32 v203, v203, v87
	v_add_f32_e32 v204, v204, v88
	v_add_f32_e32 v205, v205, v89
	v_add_f32_e32 v206, v206, v90
	v_add_f32_e32 v207, v207, v91
	v_add_f32_e32 v199, v199, v100
	v_add_f32_e32 v62, v62, v92
	v_add_f32_e32 v63, v63, v93
	v_add_f32_e32 v64, v64, v94
	v_add_f32_e32 v65, v65, v95
	v_add_f32_e32 v66, v66, v96
	v_add_f32_e32 v67, v67, v97
	v_add_f32_e32 v68, v68, v98
	v_add_f32_e32 v69, v69, v99
	v_cmp_ne_u32_e32 vcc, 0, v79
	s_and_saveexec_b64 s[84:85], vcc
	ds_write2_b32 v83, v200, v201 offset0:0 offset1:4
	ds_write2_b32 v83, v202, v203 offset0:8 offset1:12
	ds_write2_b32 v83, v204, v205 offset0:64 offset1:68
	ds_write2_b32 v83, v206, v207 offset0:72 offset1:76
	ds_write2_b32 v83, v62, v63 offset0:128 offset1:132
	ds_write2_b32 v83, v64, v65 offset0:136 offset1:140
	ds_write2_b32 v83, v66, v67 offset0:192 offset1:196
	ds_write2_b32 v83, v68, v69 offset0:200 offset1:204
	ds_write_b32 v254, v199 offset:1024
	s_mov_b64 exec, s[84:85]
	s_nop 3
